# on top of v43: router (P7) logits MFMA block rewritten by hand with a 21-deep load pipeline (7 groups of x/w fragments in flight) instead of hipcc's 2-3 loads in flight
# baseline (speedup 1.0000x reference)
; __global__ void __launch_bounds__(NTHREADS, 2) mk_fwd(Args args) {
;     ...
;         for (int unit = F.vcu; unit < NTOK / 64; unit += F.G) {
;             const int t0 = unit * 64, tg = F.wave & 1, kq = F.wave >> 1, kh = F.lane >> 5, e = F.lane & 31;
;             const bf16_t* xg = X2 + (size_t)(t0 + 32 * tg + e) * DM + kq * 512 + 32 * kh;
;             const u32x4* wp = wrb + (size_t)(kq * 8) * 512 + F.lane;
;             f32x16 acc = f32x16{};
;             u32x4 nx[4], nw[8];
; #pragma unroll
;             for (int j = 0; j < 4; ++j) nx[j] = *(const u32x4*)(xg + 8 * j);
; #pragma unroll
;             for (int q = 0; q < 8; ++q) nw[q] = wp[q * 64];
;             for (int ch = 0; ch < 8; ++ch) {
;                 u32x4 cx[4], cw[8];
; #pragma unroll
;                 for (int j = 0; j < 4; ++j) cx[j] = nx[j];
; #pragma unroll
;                 for (int q = 0; q < 8; ++q) cw[q] = nw[q];
;                 if (ch + 1 < 8) {
; #pragma unroll
;                     for (int j = 0; j < 4; ++j) nx[j] = *(const u32x4*)(xg + (ch + 1) * 64 + 8 * j);
; #pragma unroll
;                     for (int q = 0; q < 8; ++q) nw[q] = wp[(size_t)(ch + 1) * 512 + q * 64]; }
; #pragma unroll
;                 for (int j = 0; j < 4; ++j) {
;                     acc = __builtin_amdgcn_mfma_f32_32x32x16_bf16(__builtin_bit_cast(bf16x8, cx[j]), __builtin_bit_cast(bf16x8, cw[2 * j]), acc, 0, 0, 0);
;                     acc = __builtin_amdgcn_mfma_f32_32x32x16_bf16(__builtin_bit_cast(bf16x8, cx[j]), __builtin_bit_cast(bf16x8, cw[2 * j + 1]), acc, 0, 0, 0);
;                 }
;             }
.LBB0_1103:
	v_add_u32_e32 v2, s34, v163
	v_ashrrev_i32_e32 v3, 31, v2
	v_lshlrev_b64 v[2:3], 12, v[2:3]
	v_lshl_add_u64 v[18:19], v[34:35], 0, v[2:3]
	global_load_dwordx4 v[196:199], v[18:19], off
	global_load_dwordx4 v[200:203], v[36:37], off
	global_load_dwordx4 v[204:207], v[36:37], off offset:1024
	global_load_dwordx4 v[208:211], v[18:19], off offset:16
	global_load_dwordx4 v[212:215], v[36:37], off offset:2048
	global_load_dwordx4 v[216:219], v[36:37], off offset:3072
	global_load_dwordx4 v[220:223], v[18:19], off offset:32
	global_load_dwordx4 v[224:227], v[40:41], off
	global_load_dwordx4 v[228:231], v[42:43], off
	global_load_dwordx4 v[232:235], v[18:19], off offset:48
	global_load_dwordx4 v[236:239], v[44:45], off
	global_load_dwordx4 v[240:243], v[46:47], off
	global_load_dwordx4 v[170:173], v[18:19], off offset:128
	global_load_dwordx4 v[174:177], v[48:49], off
	global_load_dwordx4 v[178:181], v[50:51], off
	global_load_dwordx4 v[20:23], v[18:19], off offset:144
	global_load_dwordx4 v[24:27], v[52:53], off
	global_load_dwordx4 v[28:31], v[54:55], off
	global_load_dwordx4 v[182:185], v[18:19], off offset:160
	global_load_dwordx4 v[186:189], v[56:57], off
	global_load_dwordx4 v[244:247], v[58:59], off
	s_waitcnt vmcnt(18)
	v_mfma_f32_32x32x16_bf16 v[2:17], v[196:199], v[200:203], 0
	v_mfma_f32_32x32x16_bf16 v[2:17], v[196:199], v[204:207], v[2:17]
	global_load_dwordx4 v[196:199], v[18:19], off offset:176
	global_load_dwordx4 v[200:203], v[60:61], off
	global_load_dwordx4 v[204:207], v[62:63], off
	s_waitcnt vmcnt(18)
	v_mfma_f32_32x32x16_bf16 v[2:17], v[208:211], v[212:215], v[2:17]
	v_mfma_f32_32x32x16_bf16 v[2:17], v[208:211], v[216:219], v[2:17]
	global_load_dwordx4 v[208:211], v[18:19], off offset:256
	global_load_dwordx4 v[212:215], v[64:65], off
	global_load_dwordx4 v[216:219], v[66:67], off
	s_waitcnt vmcnt(18)
	v_mfma_f32_32x32x16_bf16 v[2:17], v[220:223], v[224:227], v[2:17]
	v_mfma_f32_32x32x16_bf16 v[2:17], v[220:223], v[228:231], v[2:17]
	global_load_dwordx4 v[220:223], v[18:19], off offset:272
	global_load_dwordx4 v[224:227], v[68:69], off
	global_load_dwordx4 v[228:231], v[70:71], off
	s_waitcnt vmcnt(18)
	v_mfma_f32_32x32x16_bf16 v[2:17], v[232:235], v[236:239], v[2:17]
	v_mfma_f32_32x32x16_bf16 v[2:17], v[232:235], v[240:243], v[2:17]
	global_load_dwordx4 v[232:235], v[18:19], off offset:288
	global_load_dwordx4 v[236:239], v[72:73], off
	global_load_dwordx4 v[240:243], v[74:75], off
	s_waitcnt vmcnt(18)
	v_mfma_f32_32x32x16_bf16 v[2:17], v[170:173], v[174:177], v[2:17]
	v_mfma_f32_32x32x16_bf16 v[2:17], v[170:173], v[178:181], v[2:17]
	global_load_dwordx4 v[170:173], v[18:19], off offset:304
	global_load_dwordx4 v[174:177], v[76:77], off
	global_load_dwordx4 v[178:181], v[78:79], off
	s_waitcnt vmcnt(18)
	v_mfma_f32_32x32x16_bf16 v[2:17], v[20:23], v[24:27], v[2:17]
	v_mfma_f32_32x32x16_bf16 v[2:17], v[20:23], v[28:31], v[2:17]
	global_load_dwordx4 v[20:23], v[18:19], off offset:384
	global_load_dwordx4 v[24:27], v[80:81], off
	global_load_dwordx4 v[28:31], v[82:83], off
	s_waitcnt vmcnt(18)
	v_mfma_f32_32x32x16_bf16 v[2:17], v[182:185], v[186:189], v[2:17]
	v_mfma_f32_32x32x16_bf16 v[2:17], v[182:185], v[244:247], v[2:17]
	global_load_dwordx4 v[182:185], v[18:19], off offset:400
	global_load_dwordx4 v[186:189], v[84:85], off
	global_load_dwordx4 v[244:247], v[86:87], off
	s_waitcnt vmcnt(18)
	v_mfma_f32_32x32x16_bf16 v[2:17], v[196:199], v[200:203], v[2:17]
	v_mfma_f32_32x32x16_bf16 v[2:17], v[196:199], v[204:207], v[2:17]
	global_load_dwordx4 v[196:199], v[18:19], off offset:416
	global_load_dwordx4 v[200:203], v[88:89], off
	global_load_dwordx4 v[204:207], v[90:91], off
	s_waitcnt vmcnt(18)
	v_mfma_f32_32x32x16_bf16 v[2:17], v[208:211], v[212:215], v[2:17]
	v_mfma_f32_32x32x16_bf16 v[2:17], v[208:211], v[216:219], v[2:17]
	global_load_dwordx4 v[208:211], v[18:19], off offset:432
	global_load_dwordx4 v[212:215], v[92:93], off
	global_load_dwordx4 v[216:219], v[94:95], off
	s_waitcnt vmcnt(18)
	v_mfma_f32_32x32x16_bf16 v[2:17], v[220:223], v[224:227], v[2:17]
	v_mfma_f32_32x32x16_bf16 v[2:17], v[220:223], v[228:231], v[2:17]
	global_load_dwordx4 v[220:223], v[18:19], off offset:512
	global_load_dwordx4 v[224:227], v[96:97], off
	global_load_dwordx4 v[228:231], v[98:99], off
	s_waitcnt vmcnt(18)
	v_mfma_f32_32x32x16_bf16 v[2:17], v[232:235], v[236:239], v[2:17]
	v_mfma_f32_32x32x16_bf16 v[2:17], v[232:235], v[240:243], v[2:17]
	global_load_dwordx4 v[232:235], v[18:19], off offset:528
	global_load_dwordx4 v[236:239], v[100:101], off
	global_load_dwordx4 v[240:243], v[102:103], off
	s_waitcnt vmcnt(18)
	v_mfma_f32_32x32x16_bf16 v[2:17], v[170:173], v[174:177], v[2:17]
	v_mfma_f32_32x32x16_bf16 v[2:17], v[170:173], v[178:181], v[2:17]
	global_load_dwordx4 v[170:173], v[18:19], off offset:544
	global_load_dwordx4 v[174:177], v[104:105], off
	global_load_dwordx4 v[178:181], v[106:107], off
	s_waitcnt vmcnt(18)
	v_mfma_f32_32x32x16_bf16 v[2:17], v[20:23], v[24:27], v[2:17]
	v_mfma_f32_32x32x16_bf16 v[2:17], v[20:23], v[28:31], v[2:17]
	global_load_dwordx4 v[20:23], v[18:19], off offset:560
	global_load_dwordx4 v[24:27], v[108:109], off
	global_load_dwordx4 v[28:31], v[110:111], off
	s_waitcnt vmcnt(18)
	v_mfma_f32_32x32x16_bf16 v[2:17], v[182:185], v[186:189], v[2:17]
	v_mfma_f32_32x32x16_bf16 v[2:17], v[182:185], v[244:247], v[2:17]
	global_load_dwordx4 v[182:185], v[18:19], off offset:640
	global_load_dwordx4 v[186:189], v[112:113], off
	global_load_dwordx4 v[244:247], v[114:115], off
	s_waitcnt vmcnt(18)
; __device__ __forceinline__ int crow(int r, int hi) { return (r & 3) + 8 * (r >> 2) + 4 * hi; }
; __global__ void __launch_bounds__(NTHREADS, 2) mk_fwd(Args args) {
;     ...
;             for (int ch = 0; ch < 8; ++ch) {
;                 u32x4 cx[4], cw[8];
; #pragma unroll
;                 for (int j = 0; j < 4; ++j) cx[j] = nx[j];
; #pragma unroll
;                 for (int q = 0; q < 8; ++q) cw[q] = nw[q];
;                 if (ch + 1 < 8) {
; #pragma unroll
;                     for (int j = 0; j < 4; ++j) nx[j] = *(const u32x4*)(xg + (ch + 1) * 64 + 8 * j);
; #pragma unroll
;                     for (int q = 0; q < 8; ++q) nw[q] = wp[(size_t)(ch + 1) * 512 + q * 64]; }
; #pragma unroll
;                 for (int j = 0; j < 4; ++j) {
;                     acc = __builtin_amdgcn_mfma_f32_32x32x16_bf16(__builtin_bit_cast(bf16x8, cx[j]), __builtin_bit_cast(bf16x8, cw[2 * j]), acc, 0, 0, 0);
;                     acc = __builtin_amdgcn_mfma_f32_32x32x16_bf16(__builtin_bit_cast(bf16x8, cx[j]), __builtin_bit_cast(bf16x8, cw[2 * j + 1]), acc, 0, 0, 0);
;                 }
;             }
;             if (F.tid < 32) hist[F.tid] = 0;
; #pragma unroll
;             for (int r = 0; r < 16; ++r) part[(kq * 64 + 32 * tg + att::crow(r, kh)) * 33 + e] = acc[r];
;             __syncthreads();
	v_mfma_f32_32x32x16_bf16 v[2:17], v[196:199], v[200:203], v[2:17]
	v_mfma_f32_32x32x16_bf16 v[2:17], v[196:199], v[204:207], v[2:17]
	global_load_dwordx4 v[196:199], v[18:19], off offset:656
	global_load_dwordx4 v[200:203], v[116:117], off
	global_load_dwordx4 v[204:207], v[118:119], off
	s_waitcnt vmcnt(18)
	v_mfma_f32_32x32x16_bf16 v[2:17], v[208:211], v[212:215], v[2:17]
	v_mfma_f32_32x32x16_bf16 v[2:17], v[208:211], v[216:219], v[2:17]
	global_load_dwordx4 v[208:211], v[18:19], off offset:672
	global_load_dwordx4 v[212:215], v[120:121], off
	global_load_dwordx4 v[216:219], v[122:123], off
	s_waitcnt vmcnt(18)
	v_mfma_f32_32x32x16_bf16 v[2:17], v[220:223], v[224:227], v[2:17]
	v_mfma_f32_32x32x16_bf16 v[2:17], v[220:223], v[228:231], v[2:17]
	global_load_dwordx4 v[220:223], v[18:19], off offset:688
	global_load_dwordx4 v[224:227], v[124:125], off
	global_load_dwordx4 v[228:231], v[126:127], off
	s_waitcnt vmcnt(18)
	v_mfma_f32_32x32x16_bf16 v[2:17], v[232:235], v[236:239], v[2:17]
	v_mfma_f32_32x32x16_bf16 v[2:17], v[232:235], v[240:243], v[2:17]
	global_load_dwordx4 v[232:235], v[18:19], off offset:768
	global_load_dwordx4 v[236:239], v[128:129], off
	global_load_dwordx4 v[240:243], v[130:131], off
	s_waitcnt vmcnt(18)
	v_mfma_f32_32x32x16_bf16 v[2:17], v[170:173], v[174:177], v[2:17]
	v_mfma_f32_32x32x16_bf16 v[2:17], v[170:173], v[178:181], v[2:17]
	global_load_dwordx4 v[170:173], v[18:19], off offset:784
	global_load_dwordx4 v[174:177], v[132:133], off
	global_load_dwordx4 v[178:181], v[134:135], off
	s_waitcnt vmcnt(18)
	v_mfma_f32_32x32x16_bf16 v[2:17], v[20:23], v[24:27], v[2:17]
	v_mfma_f32_32x32x16_bf16 v[2:17], v[20:23], v[28:31], v[2:17]
	global_load_dwordx4 v[20:23], v[18:19], off offset:800
	global_load_dwordx4 v[24:27], v[136:137], off
	global_load_dwordx4 v[28:31], v[138:139], off
	s_waitcnt vmcnt(18)
	v_mfma_f32_32x32x16_bf16 v[2:17], v[182:185], v[186:189], v[2:17]
	v_mfma_f32_32x32x16_bf16 v[2:17], v[182:185], v[244:247], v[2:17]
	global_load_dwordx4 v[182:185], v[18:19], off offset:816
	global_load_dwordx4 v[186:189], v[140:141], off
	global_load_dwordx4 v[244:247], v[142:143], off
	s_waitcnt vmcnt(18)
	v_mfma_f32_32x32x16_bf16 v[2:17], v[196:199], v[200:203], v[2:17]
	v_mfma_f32_32x32x16_bf16 v[2:17], v[196:199], v[204:207], v[2:17]
	global_load_dwordx4 v[196:199], v[18:19], off offset:896
	global_load_dwordx4 v[200:203], v[144:145], off
	global_load_dwordx4 v[204:207], v[146:147], off
	s_waitcnt vmcnt(18)
	v_mfma_f32_32x32x16_bf16 v[2:17], v[208:211], v[212:215], v[2:17]
	v_mfma_f32_32x32x16_bf16 v[2:17], v[208:211], v[216:219], v[2:17]
	global_load_dwordx4 v[208:211], v[18:19], off offset:912
	global_load_dwordx4 v[212:215], v[148:149], off
	global_load_dwordx4 v[216:219], v[150:151], off
	s_waitcnt vmcnt(18)
	v_mfma_f32_32x32x16_bf16 v[2:17], v[220:223], v[224:227], v[2:17]
	v_mfma_f32_32x32x16_bf16 v[2:17], v[220:223], v[228:231], v[2:17]
	global_load_dwordx4 v[220:223], v[18:19], off offset:928
	global_load_dwordx4 v[224:227], v[152:153], off
	global_load_dwordx4 v[228:231], v[154:155], off
	s_waitcnt vmcnt(18)
	v_mfma_f32_32x32x16_bf16 v[2:17], v[232:235], v[236:239], v[2:17]
	v_mfma_f32_32x32x16_bf16 v[2:17], v[232:235], v[240:243], v[2:17]
	global_load_dwordx4 v[232:235], v[18:19], off offset:944
	global_load_dwordx4 v[236:239], v[156:157], off
	global_load_dwordx4 v[240:243], v[158:159], off
	s_waitcnt vmcnt(18)
	v_mfma_f32_32x32x16_bf16 v[2:17], v[170:173], v[174:177], v[2:17]
	v_mfma_f32_32x32x16_bf16 v[2:17], v[170:173], v[178:181], v[2:17]
	s_waitcnt vmcnt(15)
	v_mfma_f32_32x32x16_bf16 v[2:17], v[20:23], v[24:27], v[2:17]
	v_mfma_f32_32x32x16_bf16 v[2:17], v[20:23], v[28:31], v[2:17]
	s_waitcnt vmcnt(12)
	v_mfma_f32_32x32x16_bf16 v[2:17], v[182:185], v[186:189], v[2:17]
	v_mfma_f32_32x32x16_bf16 v[2:17], v[182:185], v[244:247], v[2:17]
	s_waitcnt vmcnt(9)
	v_mfma_f32_32x32x16_bf16 v[2:17], v[196:199], v[200:203], v[2:17]
	v_mfma_f32_32x32x16_bf16 v[2:17], v[196:199], v[204:207], v[2:17]
	s_waitcnt vmcnt(6)
	v_mfma_f32_32x32x16_bf16 v[2:17], v[208:211], v[212:215], v[2:17]
	v_mfma_f32_32x32x16_bf16 v[2:17], v[208:211], v[216:219], v[2:17]
	s_waitcnt vmcnt(3)
	v_mfma_f32_32x32x16_bf16 v[2:17], v[220:223], v[224:227], v[2:17]
	v_mfma_f32_32x32x16_bf16 v[2:17], v[220:223], v[228:231], v[2:17]
	s_waitcnt vmcnt(0)
	v_mfma_f32_32x32x16_bf16 v[2:17], v[232:235], v[236:239], v[2:17]
	v_mfma_f32_32x32x16_bf16 v[2:17], v[232:235], v[240:243], v[2:17]
	s_and_saveexec_b64 s[4:5], s[0:1]
	ds_write_b32 v1, v33 offset:34816
	s_or_b64 exec, exec, s[4:5]
	s_nop 8
	ds_write2_b32 v164, v2, v3 offset1:33
	ds_write2_b32 v164, v4, v5 offset0:66 offset1:99
	v_add_u32_e32 v2, 0x400, v164
	ds_write2_b32 v2, v6, v7 offset0:8 offset1:41
	ds_write2_b32 v2, v8, v9 offset0:74 offset1:107
	v_add_u32_e32 v2, 0x800, v164
	ds_write2_b32 v2, v10, v11 offset0:16 offset1:49
	ds_write2_b32 v2, v12, v13 offset0:82 offset1:115
	v_add_u32_e32 v2, 0xc00, v164
	s_andn2_b64 vcc, exec, s[14:15]
	ds_write2_b32 v2, v14, v15 offset0:24 offset1:57
	ds_write2_b32 v2, v16, v17 offset0:90 offset1:123
	s_waitcnt lgkmcnt(0)
	s_barrier
	s_cbranch_vccnz .LBB0_1102
; __global__ void __launch_bounds__(NTHREADS, 2) mk_fwd(Args args) {
;     ...
;             if (F.wave == 0) {
;                 const int t = t0 + F.lane;
;                 const float rs = 1.0f / sqrtf(((const float*)(F.ctl + CW_SSQ2))[t] * (1.0f / DM) + RMS_EPS);
;                 float lg[32];
; #pragma unroll
;                 for (int j = 0; j < 32; ++j) lg[j] = rs * ((part[(0 * 64 + F.lane) * 33 + j] + part[(1 * 64 + F.lane) * 33 + j]) + (part[(2 * 64 + F.lane) * 33 + j] + part[(3 * 64 + F.lane) * 33 + j])) + F.b_router[j];
	v_add_u32_e32 v160, s34, v190
	v_ashrrev_i32_e32 v161, 31, v160
	v_lshl_add_u64 v[2:3], v[160:161], 2, s[18:19]
	global_load_dword v191, v[2:3], off
	v_readlane_b32 s56, v254, 11
	v_readlane_b32 s68, v254, 23
	v_readlane_b32 s69, v254, 24
	s_nop 4
	global_load_dwordx4 v[4:7], v33, s[68:69] offset:48
	global_load_dwordx4 v[8:11], v33, s[68:69] offset:32
	global_load_dwordx4 v[12:15], v33, s[68:69] offset:16
	global_load_dwordx4 v[16:19], v33, s[68:69]
	v_add_u32_e32 v26, 0x2100, v162
	v_add_u32_e32 v28, 0x4200, v162
	v_add_u32_e32 v30, 0x6300, v162
	v_add_u32_e32 v170, 0x2108, v162
	v_add_u32_e32 v172, 0x4208, v162
	v_add_u32_e32 v174, 0x6308, v162
	v_add_u32_e32 v176, 0x2110, v162
	v_add_u32_e32 v178, 0x4210, v162
	v_add_u32_e32 v180, 0x6310, v162
	ds_read2_b32 v[2:3], v162 offset1:1
	ds_read2_b32 v[20:21], v162 offset0:2 offset1:3
	ds_read2_b32 v[22:23], v162 offset0:4 offset1:5
	ds_read2_b32 v[24:25], v162 offset0:6 offset1:7
	v_add_u32_e32 v182, 0x2118, v162
	v_add_u32_e32 v184, 0x4218, v162
	v_add_u32_e32 v186, 0x6318, v162
	ds_read2_b32 v[26:27], v26 offset1:1
	ds_read2_b32 v[28:29], v28 offset1:1
	ds_read2_b32 v[30:31], v30 offset1:1
	ds_read2_b32 v[170:171], v170 offset1:1
	ds_read2_b32 v[172:173], v172 offset1:1
	ds_read2_b32 v[174:175], v174 offset1:1
	ds_read2_b32 v[176:177], v176 offset1:1
	ds_read2_b32 v[178:179], v178 offset1:1
	ds_read2_b32 v[180:181], v180 offset1:1
	ds_read2_b32 v[182:183], v182 offset1:1
	ds_read2_b32 v[184:185], v184 offset1:1
	ds_read2_b32 v[186:187], v186 offset1:1
	s_waitcnt lgkmcnt(14)
	v_mov_b32_e32 v188, v2
	v_mov_b32_e32 v2, v20
	s_waitcnt lgkmcnt(10)
	v_mov_b32_e32 v189, v28
	v_mov_b32_e32 v192, v26
	s_waitcnt lgkmcnt(9)
	v_mov_b32_e32 v193, v30
	v_mov_b32_e32 v28, v3
	v_mov_b32_e32 v30, v27
	s_waitcnt lgkmcnt(7)
	v_mov_b32_e32 v3, v172
	v_mov_b32_e32 v26, v170
	s_waitcnt lgkmcnt(6)
	v_mov_b32_e32 v27, v174
	v_pk_add_f32 v[2:3], v[2:3], v[26:27]
	v_mov_b32_e32 v20, v22
	v_mov_b32_e32 v22, v24
	v_mov_b32_e32 v172, v21
	s_waitcnt lgkmcnt(4)
	v_mov_b32_e32 v21, v178
	v_mov_b32_e32 v178, v23
	s_waitcnt lgkmcnt(1)
	v_mov_b32_e32 v23, v184
	v_mov_b32_e32 v184, v25
	v_pk_add_f32 v[24:25], v[188:189], v[192:193]
	v_pk_add_f32 v[28:29], v[28:29], v[30:31]
	v_add_f32_e32 v2, v2, v3
	v_add_f32_e32 v24, v24, v25
	v_add_f32_e32 v25, v28, v29
	v_mov_b32_e32 v174, v171
	v_mov_b32_e32 v170, v176
	v_mov_b32_e32 v171, v180
	v_mov_b32_e32 v180, v177
	v_pk_add_f32 v[26:27], v[172:173], v[174:175]
	v_pk_add_f32 v[20:21], v[20:21], v[170:171]
	v_pk_add_f32 v[30:31], v[178:179], v[180:181]
	v_add_f32_e32 v26, v26, v27
	v_add_f32_e32 v20, v20, v21
	v_add_f32_e32 v21, v30, v31
	v_mov_b32_e32 v176, v182
	s_waitcnt lgkmcnt(0)
	v_mov_b32_e32 v177, v186
	v_pk_add_f32 v[22:23], v[22:23], v[176:177]
	v_mov_b32_e32 v186, v183
	v_add_f32_e32 v22, v22, v23
	v_add_u32_e32 v173, 0x4230, v162
	v_readlane_b32 s57, v254, 12
	v_readlane_b32 s58, v254, 13
	v_readlane_b32 s59, v254, 14
	v_readlane_b32 s60, v254, 15
	v_readlane_b32 s61, v254, 16
	v_readlane_b32 s62, v254, 17
	v_readlane_b32 s63, v254, 18
	v_readlane_b32 s64, v254, 19
	v_readlane_b32 s65, v254, 20
	v_readlane_b32 s66, v254, 21
	v_readlane_b32 s67, v254, 22
	v_readlane_b32 s70, v254, 25
	v_readlane_b32 s71, v254, 26
	s_waitcnt vmcnt(4)
	v_fmamk_f32 v3, v191, 0x3a000000, v165
	v_mul_f32_e32 v28, 0x4f800000, v3
	v_cmp_gt_f32_e32 vcc, s49, v3
	s_nop 1
	v_cndmask_b32_e32 v3, v3, v28, vcc
	v_sqrt_f32_e32 v28, v3
	s_nop 0
	v_add_u32_e32 v27, -1, v28
	v_add_u32_e32 v29, 1, v28
	v_fma_f32 v30, -v27, v28, v3
	v_fma_f32 v31, -v29, v28, v3
	v_cmp_ge_f32_e64 s[4:5], 0, v30
	s_nop 1
	v_cndmask_b32_e64 v27, v28, v27, s[4:5]
	v_cmp_lt_f32_e64 s[4:5], 0, v31
	s_nop 1
	v_cndmask_b32_e64 v27, v27, v29, s[4:5]
	v_mul_f32_e32 v28, 0x37800000, v27
	v_cndmask_b32_e32 v27, v27, v28, vcc
	v_cmp_class_f32_e32 vcc, v3, v167
	s_nop 1
	v_cndmask_b32_e32 v3, v27, v3, vcc
	v_div_scale_f32 v27, s[4:5], v3, v3, 1.0
	v_rcp_f32_e32 v28, v27
	v_div_scale_f32 v23, vcc, 1.0, v3, 1.0
	v_fma_f32 v29, -v27, v28, 1.0
	v_fmac_f32_e32 v28, v29, v28
	v_mul_f32_e32 v29, v23, v28
	v_fma_f32 v30, -v27, v29, v23
	v_fmac_f32_e32 v29, v30, v28
	v_fma_f32 v23, -v27, v29, v23
	v_div_fmas_f32 v23, v23, v28, v29
	v_div_fixup_f32 v170, v23, v3, 1.0
	s_waitcnt vmcnt(0)
	v_fma_f32 v171, v170, v25, v17
	v_fma_f32 v17, v170, v2, v18
	v_pk_add_f32 v[2:3], v[184:185], v[186:187]
	v_fma_f32 v172, v170, v24, v16
	v_add_f32_e32 v2, v2, v3
	v_fmac_f32_e32 v15, v170, v2
	ds_read2_b32 v[2:3], v162 offset0:8 offset1:9
	v_fma_f32 v16, v170, v20, v12
	v_fma_f32 v12, v170, v22, v14
	v_add_u32_e32 v14, 0x2120, v162
	v_add_u32_e32 v18, 0x4220, v162
	v_add_u32_e32 v20, 0x6320, v162
	ds_read2_b32 v[28:29], v14 offset1:1
	ds_read2_b32 v[30:31], v18 offset1:1
	ds_read2_b32 v[174:175], v20 offset1:1
	ds_read2_b32 v[176:177], v162 offset0:10 offset1:11
	ds_read2_b32 v[178:179], v162 offset0:12 offset1:13
	ds_read2_b32 v[180:181], v162 offset0:14 offset1:15
	v_fma_f32 v13, v170, v21, v13
	s_waitcnt lgkmcnt(6)
	v_mov_b32_e32 v20, v2
	v_add_u32_e32 v2, 0x2128, v162
	s_waitcnt lgkmcnt(4)
	v_mov_b32_e32 v21, v30
	v_mov_b32_e32 v22, v28
	s_waitcnt lgkmcnt(3)
	v_mov_b32_e32 v23, v174
	v_fmac_f32_e32 v19, v170, v26
	ds_read2_b32 v[182:183], v2 offset1:1
	v_pk_add_f32 v[184:185], v[20:21], v[22:23]
	global_load_dwordx4 v[20:23], v33, s[68:69] offset:80
	global_load_dwordx4 v[24:27], v33, s[68:69] offset:64
	v_add_f32_e32 v2, v184, v185
	v_mov_b32_e32 v30, v3
	v_mov_b32_e32 v174, v29
	v_fma_f32 v14, v170, v2, v8
	v_pk_add_f32 v[2:3], v[30:31], v[174:175]
	v_add_u32_e32 v30, 0x2130, v162
	v_add_f32_e32 v2, v2, v3
	v_fma_f32 v18, v170, v2, v9
	v_add_u32_e32 v2, 0x4228, v162
	ds_read2_b32 v[2:3], v2 offset1:1
	v_add_u32_e32 v9, 0x6328, v162
	ds_read2_b32 v[28:29], v9 offset1:1
	ds_read2_b32 v[30:31], v30 offset1:1
	ds_read2_b32 v[174:175], v173 offset1:1
	s_waitcnt lgkmcnt(7)
; __global__ void __launch_bounds__(NTHREADS, 2) mk_fwd(Args args) {
;     ...
;                 const float rs = 1.0f / sqrtf(((const float*)(F.ctl + CW_SSQ2))[t] * (1.0f / DM) + RMS_EPS);
;                 float lg[32];
; #pragma unroll
;                 for (int j = 0; j < 32; ++j) lg[j] = rs * ((part[(0 * 64 + F.lane) * 33 + j] + part[(1 * 64 + F.lane) * 33 + j]) + (part[(2 * 64 + F.lane) * 33 + j] + part[(3 * 64 + F.lane) * 33 + j])) + F.b_router[j];
	v_mov_b32_e32 v8, v176
	s_waitcnt lgkmcnt(4)
	v_mov_b32_e32 v184, v182
	s_waitcnt lgkmcnt(3)
	v_mov_b32_e32 v9, v2
	s_waitcnt lgkmcnt(2)
	v_mov_b32_e32 v185, v28
	v_pk_add_f32 v[8:9], v[8:9], v[184:185]
	v_mov_b32_e32 v28, v183
	v_add_f32_e32 v2, v8, v9
	v_fma_f32 v10, v170, v2, v10
	v_mov_b32_e32 v2, v177
	v_pk_add_f32 v[2:3], v[2:3], v[28:29]
	v_add_u32_e32 v29, 0x2138, v162
	v_add_f32_e32 v2, v2, v3
	v_fmac_f32_e32 v11, v170, v2
	v_add_u32_e32 v2, 0x6330, v162
	ds_read2_b32 v[2:3], v2 offset1:1
	v_mov_b32_e32 v8, v178
	s_waitcnt lgkmcnt(1)
	v_mov_b32_e32 v9, v174
	v_mov_b32_e32 v28, v30
	v_add_u32_e32 v30, 0x4238, v162
	v_add_u32_e32 v173, 0x6338, v162
	ds_read2_b32 v[176:177], v29 offset1:1
	ds_read2_b32 v[182:183], v30 offset1:1
	ds_read2_b32 v[184:185], v173 offset1:1
	s_waitcnt lgkmcnt(3)
	v_mov_b32_e32 v29, v2
	v_pk_add_f32 v[8:9], v[8:9], v[28:29]
	v_mov_b32_e32 v174, v179
	v_add_f32_e32 v2, v8, v9
	v_fma_f32 v173, v170, v2, v4
	v_mov_b32_e32 v2, v31
	v_pk_add_f32 v[2:3], v[174:175], v[2:3]
	s_waitcnt lgkmcnt(2)
	v_mov_b32_e32 v4, v176
	v_add_f32_e32 v2, v2, v3
	v_fma_f32 v191, v170, v2, v5
	v_mov_b32_e32 v2, v180
	s_waitcnt lgkmcnt(1)
	v_mov_b32_e32 v3, v182
	s_waitcnt lgkmcnt(0)
	v_mov_b32_e32 v5, v184
	v_pk_add_f32 v[2:3], v[2:3], v[4:5]
	v_mov_b32_e32 v182, v181
	v_add_f32_e32 v2, v2, v3
	v_mov_b32_e32 v184, v177
	v_fma_f32 v6, v170, v2, v6
	v_pk_add_f32 v[2:3], v[182:183], v[184:185]
	ds_read2_b32 v[8:9], v162 offset0:16 offset1:17
	v_add_f32_e32 v2, v2, v3
	v_fmac_f32_e32 v7, v170, v2
	v_add_u32_e32 v2, 0x2140, v162
	v_add_u32_e32 v3, 0x4240, v162
	ds_read2_b32 v[174:175], v2 offset1:1
	ds_read2_b32 v[176:177], v3 offset1:1
	v_add_u32_e32 v2, 0x6340, v162
	v_add_u32_e32 v3, 0x2148, v162
	ds_read2_b32 v[178:179], v162 offset0:18 offset1:19
	ds_read2_b32 v[180:181], v162 offset0:20 offset1:21
	ds_read2_b32 v[182:183], v162 offset0:22 offset1:23
	ds_read2_b32 v[186:187], v2 offset1:1
	ds_read2_b32 v[188:189], v3 offset1:1
	global_load_dwordx4 v[2:5], v33, s[68:69] offset:112
	global_load_dwordx4 v[28:31], v33, s[68:69] offset:96
	s_waitcnt lgkmcnt(7)
	v_mov_b32_e32 v184, v8
	s_waitcnt lgkmcnt(5)
	v_mov_b32_e32 v185, v176
	v_mov_b32_e32 v192, v174
	s_waitcnt lgkmcnt(1)
	v_mov_b32_e32 v193, v186
	v_pk_add_f32 v[184:185], v[184:185], v[192:193]
	v_mov_b32_e32 v176, v9
	v_add_f32_e32 v8, v184, v185
	v_mov_b32_e32 v186, v175
	s_waitcnt vmcnt(2)
	v_fma_f32 v192, v170, v8, v24
	v_pk_add_f32 v[8:9], v[176:177], v[186:187]
	v_add_u32_e32 v176, 0x2150, v162
	v_add_f32_e32 v8, v8, v9
	v_fma_f32 v193, v170, v8, v25
	v_add_u32_e32 v8, 0x4248, v162
	ds_read2_b32 v[8:9], v8 offset1:1
	v_add_u32_e32 v25, 0x6348, v162
	v_mov_b32_e32 v24, v178
	v_add_u32_e32 v178, 0x4250, v162
	ds_read2_b32 v[174:175], v25 offset1:1
	ds_read2_b32 v[176:177], v176 offset1:1
	ds_read2_b32 v[184:185], v178 offset1:1
	s_waitcnt lgkmcnt(3)
	v_mov_b32_e32 v25, v8
	v_mov_b32_e32 v186, v188
	s_waitcnt lgkmcnt(2)
	v_mov_b32_e32 v187, v174
	v_pk_add_f32 v[24:25], v[24:25], v[186:187]
	v_mov_b32_e32 v174, v189
	v_add_f32_e32 v8, v24, v25
	v_fma_f32 v26, v170, v8, v26
	v_mov_b32_e32 v8, v179
	v_pk_add_f32 v[8:9], v[8:9], v[174:175]
	v_add_u32_e32 v175, 0x2158, v162
	v_add_f32_e32 v8, v8, v9
	v_fmac_f32_e32 v27, v170, v8
	v_add_u32_e32 v8, 0x6350, v162
	ds_read2_b32 v[8:9], v8 offset1:1
	v_mov_b32_e32 v24, v180
	s_waitcnt lgkmcnt(1)
	v_mov_b32_e32 v25, v184
	v_mov_b32_e32 v174, v176
	v_add_u32_e32 v176, 0x4258, v162
	v_add_u32_e32 v180, 0x6358, v162
	ds_read2_b32 v[178:179], v175 offset1:1
	ds_read2_b32 v[186:187], v176 offset1:1
	ds_read2_b32 v[188:189], v180 offset1:1
	s_waitcnt lgkmcnt(3)
	v_mov_b32_e32 v175, v8
	v_pk_add_f32 v[24:25], v[24:25], v[174:175]
	v_mov_b32_e32 v184, v181
	v_add_f32_e32 v8, v24, v25
	v_fma_f32 v194, v170, v8, v20
	v_mov_b32_e32 v8, v177
	v_pk_add_f32 v[8:9], v[184:185], v[8:9]
	s_waitcnt lgkmcnt(2)
	v_mov_b32_e32 v20, v178
	v_add_f32_e32 v8, v8, v9
	v_fma_f32 v195, v170, v8, v21
	v_mov_b32_e32 v8, v182
	s_waitcnt lgkmcnt(1)
	v_mov_b32_e32 v9, v186
	s_waitcnt lgkmcnt(0)
	v_mov_b32_e32 v21, v188
	v_pk_add_f32 v[8:9], v[8:9], v[20:21]
	v_mov_b32_e32 v186, v183
	v_add_f32_e32 v8, v8, v9
	v_mov_b32_e32 v188, v179
	v_fma_f32 v22, v170, v8, v22
	v_pk_add_f32 v[8:9], v[186:187], v[188:189]
	v_add_u32_e32 v20, 0x2160, v162
	v_add_f32_e32 v8, v8, v9
	v_fmac_f32_e32 v23, v170, v8
	ds_read2_b32 v[8:9], v162 offset0:24 offset1:25
	v_add_u32_e32 v24, 0x4260, v162
	v_add_u32_e32 v174, 0x6360, v162
	ds_read2_b32 v[20:21], v20 offset1:1
	ds_read2_b32 v[24:25], v24 offset1:1
	ds_read2_b32 v[174:175], v174 offset1:1
	ds_read2_b32 v[176:177], v162 offset0:26 offset1:27
	ds_read2_b32 v[178:179], v162 offset0:28 offset1:29
	ds_read2_b32 v[180:181], v162 offset0:30 offset1:31
	s_waitcnt lgkmcnt(4)
	v_mov_b32_e32 v183, v24
	v_mov_b32_e32 v182, v8
	v_mov_b32_e32 v186, v20
	s_waitcnt lgkmcnt(3)
	v_mov_b32_e32 v187, v174
	v_add_u32_e32 v8, 0x2168, v162
	v_pk_add_f32 v[182:183], v[182:183], v[186:187]
	ds_read2_b32 v[184:185], v8 offset1:1
	v_add_f32_e32 v8, v182, v183
	v_mov_b32_e32 v24, v9
	v_mov_b32_e32 v174, v21
	s_waitcnt vmcnt(0)
	v_fma_f32 v186, v170, v8, v28
	v_pk_add_f32 v[8:9], v[24:25], v[174:175]
	v_add_u32_e32 v21, 0x6368, v162
	v_add_f32_e32 v8, v8, v9
	v_fma_f32 v187, v170, v8, v29
	v_add_u32_e32 v8, 0x4268, v162
	ds_read2_b32 v[8:9], v8 offset1:1
	v_add_u32_e32 v28, 0x2170, v162
	v_add_u32_e32 v174, 0x4270, v162
	ds_read2_b32 v[24:25], v21 offset1:1
	ds_read2_b32 v[28:29], v28 offset1:1
	ds_read2_b32 v[174:175], v174 offset1:1
	s_waitcnt lgkmcnt(7)
	v_mov_b32_e32 v20, v176
	s_waitcnt lgkmcnt(3)
	v_mov_b32_e32 v21, v8
	v_mov_b32_e32 v182, v184
	s_waitcnt lgkmcnt(2)
; __global__ void __launch_bounds__(NTHREADS, 2) mk_fwd(Args args) {
;     ...
;                 for (int j = 0; j < 32; ++j) lg[j] = rs * ((part[(0 * 64 + F.lane) * 33 + j] + part[(1 * 64 + F.lane) * 33 + j]) + (part[(2 * 64 + F.lane) * 33 + j] + part[(3 * 64 + F.lane) * 33 + j])) + F.b_router[j];
;                 float tv[4]; int ti[4];
; #pragma unroll
;                 for (int k = 0; k < 4; ++k) { float best = -INFINITY; int bi = 0;
; #pragma unroll
;                     for (int j = 0; j < 32; ++j) if (lg[j] > best) { best = lg[j]; bi = j; }
; #pragma unroll
;                     for (int j = 0; j < 32; ++j) if (j == bi) lg[j] = -INFINITY;
	v_mov_b32_e32 v183, v24
	v_pk_add_f32 v[20:21], v[20:21], v[182:183]
	v_mov_b32_e32 v24, v185
	v_add_f32_e32 v8, v20, v21
	v_fma_f32 v30, v170, v8, v30
	v_mov_b32_e32 v8, v177
	v_pk_add_f32 v[8:9], v[8:9], v[24:25]
	v_add_u32_e32 v25, 0x2178, v162
	v_add_f32_e32 v8, v8, v9
	v_fmac_f32_e32 v31, v170, v8
	v_add_u32_e32 v8, 0x6370, v162
	ds_read2_b32 v[8:9], v8 offset1:1
	v_mov_b32_e32 v20, v178
	s_waitcnt lgkmcnt(1)
	v_mov_b32_e32 v21, v174
	v_mov_b32_e32 v24, v28
	v_add_u32_e32 v28, 0x4278, v162
	v_add_u32_e32 v174, 0x6378, v162
	ds_read2_b32 v[176:177], v25 offset1:1
	ds_read2_b32 v[182:183], v28 offset1:1
	ds_read2_b32 v[184:185], v174 offset1:1
	s_waitcnt lgkmcnt(3)
	v_mov_b32_e32 v25, v8
	v_pk_add_f32 v[20:21], v[20:21], v[24:25]
	v_mov_b32_e32 v174, v179
	v_add_f32_e32 v8, v20, v21
	v_fma_f32 v20, v170, v8, v2
	v_mov_b32_e32 v8, v29
	v_pk_add_f32 v[8:9], v[174:175], v[8:9]
	s_nop 0
	v_add_f32_e32 v2, v8, v9
	v_fma_f32 v21, v170, v2, v3
	v_mov_b32_e32 v2, v180
	s_waitcnt lgkmcnt(1)
	v_mov_b32_e32 v3, v182
	v_mov_b32_e32 v8, v176
	s_waitcnt lgkmcnt(0)
	v_mov_b32_e32 v9, v184
	v_pk_add_f32 v[2:3], v[2:3], v[8:9]
	v_mov_b32_e32 v182, v181
	v_add_f32_e32 v2, v2, v3
	v_mov_b32_e32 v184, v177
	v_fma_f32 v4, v170, v2, v4
	v_pk_add_f32 v[2:3], v[182:183], v[184:185]
	s_nop 0
	v_add_f32_e32 v2, v2, v3
	v_fmac_f32_e32 v5, v170, v2
	v_max_f32_e32 v2, 0xff800000, v172
	v_cmp_gt_f32_e32 vcc, v171, v2
	s_nop 1
	v_cndmask_b32_e32 v2, v2, v171, vcc
	v_cndmask_b32_e64 v3, 0, 1, vcc
	v_cmp_gt_f32_e32 vcc, v17, v2
	s_nop 1
	v_cndmask_b32_e32 v2, v2, v17, vcc
	v_cndmask_b32_e64 v3, v3, 2, vcc
	v_cmp_gt_f32_e32 vcc, v19, v2
	s_nop 1
	v_cndmask_b32_e32 v2, v2, v19, vcc
	v_cndmask_b32_e64 v3, v3, 3, vcc
	v_cmp_gt_f32_e32 vcc, v16, v2
	s_nop 1
	v_cndmask_b32_e32 v2, v2, v16, vcc
	v_cndmask_b32_e64 v3, v3, 4, vcc
	v_cmp_gt_f32_e32 vcc, v13, v2
	s_nop 1
	v_cndmask_b32_e32 v2, v2, v13, vcc
	v_cndmask_b32_e64 v3, v3, 5, vcc
	v_cmp_gt_f32_e32 vcc, v12, v2
	s_nop 1
	v_cndmask_b32_e32 v2, v2, v12, vcc
	v_cndmask_b32_e64 v3, v3, 6, vcc
	v_cmp_gt_f32_e32 vcc, v15, v2
	s_nop 1
	v_cndmask_b32_e32 v2, v2, v15, vcc
	v_cndmask_b32_e64 v3, v3, 7, vcc
	v_cmp_gt_f32_e32 vcc, v14, v2
	s_nop 1
	v_cndmask_b32_e32 v2, v2, v14, vcc
	v_cndmask_b32_e64 v3, v3, 8, vcc
	v_cmp_gt_f32_e32 vcc, v18, v2
	s_nop 1
	v_cndmask_b32_e32 v2, v2, v18, vcc
	v_cndmask_b32_e64 v3, v3, 9, vcc
	v_cmp_gt_f32_e32 vcc, v10, v2
	s_nop 1
	v_cndmask_b32_e32 v2, v2, v10, vcc
	v_cndmask_b32_e64 v3, v3, 10, vcc
	v_cmp_gt_f32_e32 vcc, v11, v2
	s_nop 1
	v_cndmask_b32_e32 v2, v2, v11, vcc
	v_cndmask_b32_e64 v3, v3, 11, vcc
	v_cmp_gt_f32_e32 vcc, v173, v2
	s_nop 1
	v_cndmask_b32_e32 v2, v2, v173, vcc
	v_cndmask_b32_e64 v3, v3, 12, vcc
	v_cmp_gt_f32_e32 vcc, v191, v2
	s_nop 1
	v_cndmask_b32_e32 v2, v2, v191, vcc
	v_cndmask_b32_e64 v3, v3, 13, vcc
	v_cmp_gt_f32_e32 vcc, v6, v2
	s_nop 1
	v_cndmask_b32_e32 v2, v2, v6, vcc
	v_cndmask_b32_e64 v3, v3, 14, vcc
	v_cmp_gt_f32_e32 vcc, v7, v2
	s_nop 1
	v_cndmask_b32_e32 v2, v2, v7, vcc
	v_cndmask_b32_e64 v3, v3, 15, vcc
	v_cmp_gt_f32_e32 vcc, v192, v2
	s_nop 1
	v_cndmask_b32_e32 v2, v2, v192, vcc
	v_cndmask_b32_e64 v3, v3, 16, vcc
	v_cmp_gt_f32_e32 vcc, v193, v2
	s_nop 1
	v_cndmask_b32_e32 v2, v2, v193, vcc
	v_cndmask_b32_e64 v3, v3, 17, vcc
	v_cmp_gt_f32_e32 vcc, v26, v2
	s_nop 1
	v_cndmask_b32_e32 v2, v2, v26, vcc
	v_cndmask_b32_e64 v3, v3, 18, vcc
	v_cmp_gt_f32_e32 vcc, v27, v2
	s_nop 1
	v_cndmask_b32_e32 v2, v2, v27, vcc
	v_cndmask_b32_e64 v3, v3, 19, vcc
	v_cmp_gt_f32_e32 vcc, v194, v2
	s_nop 1
	v_cndmask_b32_e32 v2, v2, v194, vcc
	v_cndmask_b32_e64 v3, v3, 20, vcc
	v_cmp_gt_f32_e32 vcc, v195, v2
	s_nop 1
	v_cndmask_b32_e32 v2, v2, v195, vcc
	v_cndmask_b32_e64 v3, v3, 21, vcc
	v_cmp_gt_f32_e32 vcc, v22, v2
	s_nop 1
	v_cndmask_b32_e32 v2, v2, v22, vcc
	v_cndmask_b32_e64 v3, v3, 22, vcc
	v_cmp_gt_f32_e32 vcc, v23, v2
	s_nop 1
	v_cndmask_b32_e32 v2, v2, v23, vcc
	v_cndmask_b32_e64 v3, v3, 23, vcc
	v_cmp_gt_f32_e32 vcc, v186, v2
	s_nop 1
	v_cndmask_b32_e32 v2, v2, v186, vcc
	v_cndmask_b32_e64 v3, v3, 24, vcc
	v_cmp_gt_f32_e32 vcc, v187, v2
	s_nop 1
	v_cndmask_b32_e32 v2, v2, v187, vcc
	v_cndmask_b32_e64 v3, v3, 25, vcc
	v_cmp_gt_f32_e32 vcc, v30, v2
	s_nop 1
	v_cndmask_b32_e32 v2, v2, v30, vcc
	v_cndmask_b32_e64 v3, v3, 26, vcc
	v_cmp_gt_f32_e32 vcc, v31, v2
	s_nop 1
	v_cndmask_b32_e32 v2, v2, v31, vcc
	v_cndmask_b32_e64 v3, v3, 27, vcc
	v_cmp_gt_f32_e32 vcc, v20, v2
	s_nop 1
	v_cndmask_b32_e32 v2, v2, v20, vcc
	v_cndmask_b32_e64 v3, v3, 28, vcc
	v_cmp_gt_f32_e32 vcc, v21, v2
	s_nop 1
	v_cndmask_b32_e32 v2, v2, v21, vcc
	v_cndmask_b32_e64 v8, v3, 29, vcc
	v_cmp_gt_f32_e32 vcc, v4, v2
	s_nop 1
	v_cndmask_b32_e32 v3, v2, v4, vcc
	v_cndmask_b32_e64 v2, v8, 30, vcc
	v_cmp_gt_f32_e32 vcc, v5, v3
	s_nop 1
	v_cndmask_b32_e64 v2, v2, 31, vcc
	v_cmp_ne_u32_e64 s[4:5], 0, v2
	s_nop 1
	v_cndmask_b32_e64 v8, v168, v172, s[4:5]
	v_cmp_ne_u32_e64 s[4:5], 1, v2
	s_nop 1
	v_cndmask_b32_e64 v9, v168, v171, s[4:5]
	v_cmp_ne_u32_e64 s[4:5], 2, v2
	s_nop 1
	v_cndmask_b32_e64 v17, v168, v17, s[4:5]
	v_cmp_ne_u32_e64 s[4:5], 3, v2
	s_nop 1
	v_cndmask_b32_e64 v19, v168, v19, s[4:5]
	v_cmp_ne_u32_e64 s[4:5], 4, v2
	s_nop 1
	v_cndmask_b32_e64 v16, v168, v16, s[4:5]
	v_cmp_ne_u32_e64 s[4:5], 5, v2
	s_nop 1
	v_cndmask_b32_e64 v13, v168, v13, s[4:5]
	v_cmp_ne_u32_e64 s[4:5], 6, v2
	s_nop 1
	v_cndmask_b32_e64 v12, v168, v12, s[4:5]
	v_cmp_ne_u32_e64 s[4:5], 7, v2
	s_nop 1
	v_cndmask_b32_e64 v15, v168, v15, s[4:5]
	v_cmp_ne_u32_e64 s[4:5], 8, v2
	s_nop 1
	v_cndmask_b32_e64 v14, v168, v14, s[4:5]
	v_cmp_ne_u32_e64 s[4:5], 9, v2
	s_nop 1
	v_cndmask_b32_e64 v18, v168, v18, s[4:5]
	v_cmp_ne_u32_e64 s[4:5], 10, v2
; __global__ void __launch_bounds__(NTHREADS, 2) mk_fwd(Args args) {
;     ...
;                 for (int k = 0; k < 4; ++k) { float best = -INFINITY; int bi = 0;
; #pragma unroll
;                     for (int j = 0; j < 32; ++j) if (lg[j] > best) { best = lg[j]; bi = j; }
; #pragma unroll
;                     for (int j = 0; j < 32; ++j) if (j == bi) lg[j] = -INFINITY;
	s_nop 1
	v_cndmask_b32_e64 v10, v168, v10, s[4:5]
	v_cmp_ne_u32_e64 s[4:5], 11, v2
	s_nop 1
	v_cndmask_b32_e64 v11, v168, v11, s[4:5]
	v_cmp_ne_u32_e64 s[4:5], 12, v2
	s_nop 1
	v_cndmask_b32_e64 v24, v168, v173, s[4:5]
	v_cmp_ne_u32_e64 s[4:5], 13, v2
	s_nop 1
	v_cndmask_b32_e64 v25, v168, v191, s[4:5]
	v_cmp_ne_u32_e64 s[4:5], 14, v2
	s_nop 1
	v_cndmask_b32_e64 v28, v168, v6, s[4:5]
	v_cmp_ne_u32_e64 s[4:5], 15, v2
	s_nop 1
	v_cndmask_b32_e64 v29, v168, v7, s[4:5]
	v_cmp_ne_u32_e64 s[4:5], 16, v2
	s_nop 1
	v_cndmask_b32_e64 v171, v168, v192, s[4:5]
	v_cmp_ne_u32_e64 s[4:5], 17, v2
	s_nop 1
	v_cndmask_b32_e64 v172, v168, v193, s[4:5]
	v_cmp_ne_u32_e64 s[4:5], 18, v2
	s_nop 1
	v_cndmask_b32_e64 v26, v168, v26, s[4:5]
	v_cmp_ne_u32_e64 s[4:5], 19, v2
	s_nop 1
	v_cndmask_b32_e64 v27, v168, v27, s[4:5]
	v_cmp_ne_u32_e64 s[4:5], 20, v2
	s_nop 1
	v_cndmask_b32_e64 v173, v168, v194, s[4:5]
	v_cmp_ne_u32_e64 s[4:5], 21, v2
	s_nop 1
	v_cndmask_b32_e64 v174, v168, v195, s[4:5]
	v_cmp_ne_u32_e64 s[4:5], 22, v2
	s_nop 1
	v_cndmask_b32_e64 v22, v168, v22, s[4:5]
	v_cmp_ne_u32_e64 s[4:5], 23, v2
	s_nop 1
	v_cndmask_b32_e64 v23, v168, v23, s[4:5]
	v_cmp_ne_u32_e64 s[4:5], 24, v2
	s_nop 1
	v_cndmask_b32_e64 v175, v168, v186, s[4:5]
	v_cmp_ne_u32_e64 s[4:5], 25, v2
	s_nop 1
	v_cndmask_b32_e64 v176, v168, v187, s[4:5]
	v_cmp_ne_u32_e64 s[4:5], 26, v2
	s_nop 1
	v_cndmask_b32_e64 v30, v168, v30, s[4:5]
	v_cmp_ne_u32_e64 s[4:5], 27, v2
	s_nop 1
	v_cndmask_b32_e64 v31, v168, v31, s[4:5]
	v_cmp_ne_u32_e64 s[4:5], 28, v2
	s_nop 1
	v_cndmask_b32_e64 v20, v168, v20, s[4:5]
	v_cmp_ne_u32_e64 s[4:5], 29, v2
	s_nop 1
	v_cndmask_b32_e64 v21, v168, v21, s[4:5]
	v_cmp_ne_u32_e64 s[4:5], 30, v2
	s_nop 1
	v_cndmask_b32_e64 v177, v168, v4, s[4:5]
	v_cmp_ne_u32_e64 s[4:5], 31, v2
	v_max_f32_e32 v4, 0xff800000, v8
	s_nop 0
	v_cndmask_b32_e64 v6, v168, v5, s[4:5]
	v_cmp_gt_f32_e64 s[4:5], v9, v4
	s_nop 1
	v_cndmask_b32_e64 v4, v4, v9, s[4:5]
	v_cndmask_b32_e64 v7, 0, 1, s[4:5]
	v_cmp_gt_f32_e64 s[4:5], v17, v4
	s_nop 1
	v_cndmask_b32_e64 v4, v4, v17, s[4:5]
	v_cndmask_b32_e64 v7, v7, 2, s[4:5]
	v_cmp_gt_f32_e64 s[4:5], v19, v4
	s_nop 1
	v_cndmask_b32_e64 v4, v4, v19, s[4:5]
	v_cndmask_b32_e64 v7, v7, 3, s[4:5]
	v_cmp_gt_f32_e64 s[4:5], v16, v4
	s_nop 1
	v_cndmask_b32_e64 v4, v4, v16, s[4:5]
	v_cndmask_b32_e64 v7, v7, 4, s[4:5]
	v_cmp_gt_f32_e64 s[4:5], v13, v4
	s_nop 1
	v_cndmask_b32_e64 v4, v4, v13, s[4:5]
	v_cndmask_b32_e64 v7, v7, 5, s[4:5]
	v_cmp_gt_f32_e64 s[4:5], v12, v4
	s_nop 1
	v_cndmask_b32_e64 v4, v4, v12, s[4:5]
	v_cndmask_b32_e64 v7, v7, 6, s[4:5]
	v_cmp_gt_f32_e64 s[4:5], v15, v4
	s_nop 1
	v_cndmask_b32_e64 v4, v4, v15, s[4:5]
	v_cndmask_b32_e64 v7, v7, 7, s[4:5]
	v_cmp_gt_f32_e64 s[4:5], v14, v4
	s_nop 1
	v_cndmask_b32_e64 v4, v4, v14, s[4:5]
	v_cndmask_b32_e64 v7, v7, 8, s[4:5]
	v_cmp_gt_f32_e64 s[4:5], v18, v4
	s_nop 1
	v_cndmask_b32_e64 v4, v4, v18, s[4:5]
	v_cndmask_b32_e64 v7, v7, 9, s[4:5]
	v_cmp_gt_f32_e64 s[4:5], v10, v4
	s_nop 1
	v_cndmask_b32_e64 v4, v4, v10, s[4:5]
	v_cndmask_b32_e64 v7, v7, 10, s[4:5]
	v_cmp_gt_f32_e64 s[4:5], v11, v4
	s_nop 1
	v_cndmask_b32_e64 v4, v4, v11, s[4:5]
	v_cndmask_b32_e64 v7, v7, 11, s[4:5]
	v_cmp_gt_f32_e64 s[4:5], v24, v4
	s_nop 1
	v_cndmask_b32_e64 v4, v4, v24, s[4:5]
	v_cndmask_b32_e64 v7, v7, 12, s[4:5]
	v_cmp_gt_f32_e64 s[4:5], v25, v4
	s_nop 1
	v_cndmask_b32_e64 v4, v4, v25, s[4:5]
	v_cndmask_b32_e64 v7, v7, 13, s[4:5]
	v_cmp_gt_f32_e64 s[4:5], v28, v4
	s_nop 1
	v_cndmask_b32_e64 v4, v4, v28, s[4:5]
	v_cndmask_b32_e64 v7, v7, 14, s[4:5]
	v_cmp_gt_f32_e64 s[4:5], v29, v4
	s_nop 1
	v_cndmask_b32_e64 v4, v4, v29, s[4:5]
	v_cndmask_b32_e64 v7, v7, 15, s[4:5]
	v_cmp_gt_f32_e64 s[4:5], v171, v4
	s_nop 1
	v_cndmask_b32_e64 v4, v4, v171, s[4:5]
	v_cndmask_b32_e64 v7, v7, 16, s[4:5]
	v_cmp_gt_f32_e64 s[4:5], v172, v4
	s_nop 1
	v_cndmask_b32_e64 v4, v4, v172, s[4:5]
	v_cndmask_b32_e64 v7, v7, 17, s[4:5]
	v_cmp_gt_f32_e64 s[4:5], v26, v4
	s_nop 1
	v_cndmask_b32_e64 v4, v4, v26, s[4:5]
	v_cndmask_b32_e64 v7, v7, 18, s[4:5]
	v_cmp_gt_f32_e64 s[4:5], v27, v4
	s_nop 1
	v_cndmask_b32_e64 v4, v4, v27, s[4:5]
	v_cndmask_b32_e64 v7, v7, 19, s[4:5]
	v_cmp_gt_f32_e64 s[4:5], v173, v4
	s_nop 1
	v_cndmask_b32_e64 v4, v4, v173, s[4:5]
	v_cndmask_b32_e64 v7, v7, 20, s[4:5]
	v_cmp_gt_f32_e64 s[4:5], v174, v4
	s_nop 1
	v_cndmask_b32_e64 v4, v4, v174, s[4:5]
	v_cndmask_b32_e64 v7, v7, 21, s[4:5]
	v_cmp_gt_f32_e64 s[4:5], v22, v4
	s_nop 1
	v_cndmask_b32_e64 v4, v4, v22, s[4:5]
	v_cndmask_b32_e64 v7, v7, 22, s[4:5]
	v_cmp_gt_f32_e64 s[4:5], v23, v4
	s_nop 1
	v_cndmask_b32_e64 v4, v4, v23, s[4:5]
	v_cndmask_b32_e64 v7, v7, 23, s[4:5]
	v_cmp_gt_f32_e64 s[4:5], v175, v4
	s_nop 1
	v_cndmask_b32_e64 v4, v4, v175, s[4:5]
	v_cndmask_b32_e64 v7, v7, 24, s[4:5]
	v_cmp_gt_f32_e64 s[4:5], v176, v4
	s_nop 1
	v_cndmask_b32_e64 v4, v4, v176, s[4:5]
	v_cndmask_b32_e64 v7, v7, 25, s[4:5]
	v_cmp_gt_f32_e64 s[4:5], v30, v4
	s_nop 1
	v_cndmask_b32_e64 v4, v4, v30, s[4:5]
	v_cndmask_b32_e64 v7, v7, 26, s[4:5]
	v_cmp_gt_f32_e64 s[4:5], v31, v4
	s_nop 1
	v_cndmask_b32_e64 v4, v4, v31, s[4:5]
	v_cndmask_b32_e64 v7, v7, 27, s[4:5]
	v_cmp_gt_f32_e64 s[4:5], v20, v4
	s_nop 1
	v_cndmask_b32_e64 v4, v4, v20, s[4:5]
	v_cndmask_b32_e64 v7, v7, 28, s[4:5]
	v_cmp_gt_f32_e64 s[4:5], v21, v4
	s_nop 1
	v_cndmask_b32_e64 v4, v4, v21, s[4:5]
	v_cndmask_b32_e64 v178, v7, 29, s[4:5]
	v_cmp_gt_f32_e64 s[4:5], v177, v4
	s_nop 1
	v_cndmask_b32_e64 v7, v4, v177, s[4:5]
	v_cndmask_b32_e64 v4, v178, 30, s[4:5]
	v_cmp_gt_f32_e64 s[4:5], v6, v7
	s_nop 1
	v_cndmask_b32_e64 v4, v4, 31, s[4:5]
	v_cmp_ne_u32_e64 s[6:7], 0, v4
	s_nop 1
	v_cndmask_b32_e64 v178, v168, v8, s[6:7]
; __global__ void __launch_bounds__(NTHREADS, 2) mk_fwd(Args args) {
;     ...
;                 for (int k = 0; k < 4; ++k) { float best = -INFINITY; int bi = 0;
; #pragma unroll
;                     for (int j = 0; j < 32; ++j) if (lg[j] > best) { best = lg[j]; bi = j; }
; #pragma unroll
;                     for (int j = 0; j < 32; ++j) if (j == bi) lg[j] = -INFINITY;
	v_cmp_ne_u32_e64 s[6:7], 1, v4
	v_max_f32_e32 v8, 0xff800000, v178
	s_nop 0
	v_cndmask_b32_e64 v179, v168, v9, s[6:7]
	v_cmp_ne_u32_e64 s[6:7], 2, v4
	s_nop 1
	v_cndmask_b32_e64 v17, v168, v17, s[6:7]
	v_cmp_ne_u32_e64 s[6:7], 3, v4
	s_nop 1
	v_cndmask_b32_e64 v19, v168, v19, s[6:7]
	v_cmp_ne_u32_e64 s[6:7], 4, v4
	s_nop 1
	v_cndmask_b32_e64 v16, v168, v16, s[6:7]
	v_cmp_ne_u32_e64 s[6:7], 5, v4
	s_nop 1
	v_cndmask_b32_e64 v13, v168, v13, s[6:7]
	v_cmp_ne_u32_e64 s[6:7], 6, v4
	s_nop 1
	v_cndmask_b32_e64 v12, v168, v12, s[6:7]
	v_cmp_ne_u32_e64 s[6:7], 7, v4
	s_nop 1
	v_cndmask_b32_e64 v15, v168, v15, s[6:7]
	v_cmp_ne_u32_e64 s[6:7], 8, v4
	s_nop 1
	v_cndmask_b32_e64 v14, v168, v14, s[6:7]
	v_cmp_ne_u32_e64 s[6:7], 9, v4
	s_nop 1
	v_cndmask_b32_e64 v18, v168, v18, s[6:7]
	v_cmp_ne_u32_e64 s[6:7], 10, v4
	s_nop 1
	v_cndmask_b32_e64 v180, v168, v10, s[6:7]
	v_cmp_ne_u32_e64 s[6:7], 11, v4
	s_nop 1
	v_cndmask_b32_e64 v11, v168, v11, s[6:7]
	v_cmp_ne_u32_e64 s[6:7], 12, v4
	s_nop 1
	v_cndmask_b32_e64 v24, v168, v24, s[6:7]
	v_cmp_ne_u32_e64 s[6:7], 13, v4
	s_nop 1
	v_cndmask_b32_e64 v25, v168, v25, s[6:7]
	v_cmp_ne_u32_e64 s[6:7], 14, v4
	s_nop 1
	v_cndmask_b32_e64 v28, v168, v28, s[6:7]
	v_cmp_ne_u32_e64 s[6:7], 15, v4
	s_nop 1
	v_cndmask_b32_e64 v29, v168, v29, s[6:7]
	v_cmp_ne_u32_e64 s[6:7], 16, v4
	s_nop 1
	v_cndmask_b32_e64 v171, v168, v171, s[6:7]
	v_cmp_ne_u32_e64 s[6:7], 17, v4
	s_nop 1
	v_cndmask_b32_e64 v172, v168, v172, s[6:7]
	v_cmp_ne_u32_e64 s[6:7], 18, v4
	s_nop 1
	v_cndmask_b32_e64 v26, v168, v26, s[6:7]
	v_cmp_ne_u32_e64 s[6:7], 19, v4
	s_nop 1
	v_cndmask_b32_e64 v27, v168, v27, s[6:7]
	v_cmp_ne_u32_e64 s[6:7], 20, v4
	s_nop 1
	v_cndmask_b32_e64 v173, v168, v173, s[6:7]
	v_cmp_ne_u32_e64 s[6:7], 21, v4
	s_nop 1
	v_cndmask_b32_e64 v174, v168, v174, s[6:7]
	v_cmp_ne_u32_e64 s[6:7], 22, v4
	s_nop 1
	v_cndmask_b32_e64 v22, v168, v22, s[6:7]
	v_cmp_ne_u32_e64 s[6:7], 23, v4
	s_nop 1
	v_cndmask_b32_e64 v23, v168, v23, s[6:7]
	v_cmp_ne_u32_e64 s[6:7], 24, v4
	s_nop 1
	v_cndmask_b32_e64 v175, v168, v175, s[6:7]
	v_cmp_ne_u32_e64 s[6:7], 25, v4
	s_nop 1
	v_cndmask_b32_e64 v176, v168, v176, s[6:7]
	v_cmp_ne_u32_e64 s[6:7], 26, v4
	s_nop 1
	v_cndmask_b32_e64 v30, v168, v30, s[6:7]
	v_cmp_ne_u32_e64 s[6:7], 27, v4
	s_nop 1
	v_cndmask_b32_e64 v31, v168, v31, s[6:7]
	v_cmp_ne_u32_e64 s[6:7], 28, v4
	s_nop 1
	v_cndmask_b32_e64 v20, v168, v20, s[6:7]
	v_cmp_ne_u32_e64 s[6:7], 29, v4
	s_nop 1
	v_cndmask_b32_e64 v21, v168, v21, s[6:7]
	v_cmp_ne_u32_e64 s[6:7], 30, v4
	s_nop 1
	v_cndmask_b32_e64 v177, v168, v177, s[6:7]
	v_cmp_ne_u32_e64 s[6:7], 31, v4
	s_nop 1
	v_cndmask_b32_e64 v9, v168, v6, s[6:7]
	v_cmp_gt_f32_e64 s[6:7], v179, v8
	s_nop 1
	v_cndmask_b32_e64 v8, v8, v179, s[6:7]
	v_cndmask_b32_e64 v10, 0, 1, s[6:7]
	v_cmp_gt_f32_e64 s[6:7], v17, v8
	s_nop 1
	v_cndmask_b32_e64 v8, v8, v17, s[6:7]
	v_cndmask_b32_e64 v10, v10, 2, s[6:7]
	v_cmp_gt_f32_e64 s[6:7], v19, v8
	s_nop 1
	v_cndmask_b32_e64 v8, v8, v19, s[6:7]
	v_cndmask_b32_e64 v10, v10, 3, s[6:7]
	v_cmp_gt_f32_e64 s[6:7], v16, v8
	s_nop 1
	v_cndmask_b32_e64 v8, v8, v16, s[6:7]
	v_cndmask_b32_e64 v10, v10, 4, s[6:7]
	v_cmp_gt_f32_e64 s[6:7], v13, v8
	s_nop 1
	v_cndmask_b32_e64 v8, v8, v13, s[6:7]
	v_cndmask_b32_e64 v10, v10, 5, s[6:7]
	v_cmp_gt_f32_e64 s[6:7], v12, v8
	s_nop 1
	v_cndmask_b32_e64 v8, v8, v12, s[6:7]
	v_cndmask_b32_e64 v10, v10, 6, s[6:7]
	v_cmp_gt_f32_e64 s[6:7], v15, v8
	s_nop 1
	v_cndmask_b32_e64 v8, v8, v15, s[6:7]
	v_cndmask_b32_e64 v10, v10, 7, s[6:7]
	v_cmp_gt_f32_e64 s[6:7], v14, v8
	s_nop 1
	v_cndmask_b32_e64 v8, v8, v14, s[6:7]
	v_cndmask_b32_e64 v10, v10, 8, s[6:7]
	v_cmp_gt_f32_e64 s[6:7], v18, v8
	s_nop 1
	v_cndmask_b32_e64 v8, v8, v18, s[6:7]
	v_cndmask_b32_e64 v10, v10, 9, s[6:7]
	v_cmp_gt_f32_e64 s[6:7], v180, v8
	s_nop 1
	v_cndmask_b32_e64 v8, v8, v180, s[6:7]
	v_cndmask_b32_e64 v10, v10, 10, s[6:7]
	v_cmp_gt_f32_e64 s[6:7], v11, v8
	s_nop 1
	v_cndmask_b32_e64 v8, v8, v11, s[6:7]
	v_cndmask_b32_e64 v10, v10, 11, s[6:7]
	v_cmp_gt_f32_e64 s[6:7], v24, v8
	s_nop 1
	v_cndmask_b32_e64 v8, v8, v24, s[6:7]
	v_cndmask_b32_e64 v10, v10, 12, s[6:7]
	v_cmp_gt_f32_e64 s[6:7], v25, v8
	s_nop 1
	v_cndmask_b32_e64 v8, v8, v25, s[6:7]
	v_cndmask_b32_e64 v10, v10, 13, s[6:7]
	v_cmp_gt_f32_e64 s[6:7], v28, v8
	s_nop 1
	v_cndmask_b32_e64 v8, v8, v28, s[6:7]
	v_cndmask_b32_e64 v10, v10, 14, s[6:7]
	v_cmp_gt_f32_e64 s[6:7], v29, v8
	s_nop 1
	v_cndmask_b32_e64 v8, v8, v29, s[6:7]
	v_cndmask_b32_e64 v10, v10, 15, s[6:7]
	v_cmp_gt_f32_e64 s[6:7], v171, v8
	s_nop 1
	v_cndmask_b32_e64 v8, v8, v171, s[6:7]
	v_cndmask_b32_e64 v10, v10, 16, s[6:7]
	v_cmp_gt_f32_e64 s[6:7], v172, v8
	s_nop 1
	v_cndmask_b32_e64 v8, v8, v172, s[6:7]
	v_cndmask_b32_e64 v10, v10, 17, s[6:7]
	v_cmp_gt_f32_e64 s[6:7], v26, v8
	s_nop 1
	v_cndmask_b32_e64 v8, v8, v26, s[6:7]
	v_cndmask_b32_e64 v10, v10, 18, s[6:7]
	v_cmp_gt_f32_e64 s[6:7], v27, v8
	s_nop 1
	v_cndmask_b32_e64 v8, v8, v27, s[6:7]
	v_cndmask_b32_e64 v10, v10, 19, s[6:7]
	v_cmp_gt_f32_e64 s[6:7], v173, v8
	s_nop 1
	v_cndmask_b32_e64 v8, v8, v173, s[6:7]
	v_cndmask_b32_e64 v10, v10, 20, s[6:7]
	v_cmp_gt_f32_e64 s[6:7], v174, v8
	s_nop 1
	v_cndmask_b32_e64 v8, v8, v174, s[6:7]
	v_cndmask_b32_e64 v10, v10, 21, s[6:7]
	v_cmp_gt_f32_e64 s[6:7], v22, v8
	s_nop 1
	v_cndmask_b32_e64 v8, v8, v22, s[6:7]
	v_cndmask_b32_e64 v10, v10, 22, s[6:7]
	v_cmp_gt_f32_e64 s[6:7], v23, v8
	s_nop 1
	v_cndmask_b32_e64 v8, v8, v23, s[6:7]
	v_cndmask_b32_e64 v10, v10, 23, s[6:7]
	v_cmp_gt_f32_e64 s[6:7], v175, v8
	s_nop 1
	v_cndmask_b32_e64 v8, v8, v175, s[6:7]
	v_cndmask_b32_e64 v10, v10, 24, s[6:7]
	v_cmp_gt_f32_e64 s[6:7], v176, v8
	s_nop 1
	v_cndmask_b32_e64 v8, v8, v176, s[6:7]
; __global__ void __launch_bounds__(NTHREADS, 2) mk_fwd(Args args) {
;     ...
;                 for (int k = 0; k < 4; ++k) { float best = -INFINITY; int bi = 0;
; #pragma unroll
;                     for (int j = 0; j < 32; ++j) if (lg[j] > best) { best = lg[j]; bi = j; }
; #pragma unroll
;                     for (int j = 0; j < 32; ++j) if (j == bi) lg[j] = -INFINITY;
;                     tv[k] = best; ti[k] = bi; }
	v_cndmask_b32_e64 v10, v10, 25, s[6:7]
	v_cmp_gt_f32_e64 s[6:7], v30, v8
	s_nop 1
	v_cndmask_b32_e64 v8, v8, v30, s[6:7]
	v_cndmask_b32_e64 v10, v10, 26, s[6:7]
	v_cmp_gt_f32_e64 s[6:7], v31, v8
	s_nop 1
	v_cndmask_b32_e64 v8, v8, v31, s[6:7]
	v_cndmask_b32_e64 v10, v10, 27, s[6:7]
	v_cmp_gt_f32_e64 s[6:7], v20, v8
	s_nop 1
	v_cndmask_b32_e64 v8, v8, v20, s[6:7]
	v_cndmask_b32_e64 v10, v10, 28, s[6:7]
	v_cmp_gt_f32_e64 s[6:7], v21, v8
	s_nop 1
	v_cndmask_b32_e64 v8, v8, v21, s[6:7]
	v_cndmask_b32_e64 v181, v10, 29, s[6:7]
	v_cmp_gt_f32_e64 s[6:7], v177, v8
	s_nop 1
	v_cndmask_b32_e64 v10, v8, v177, s[6:7]
	v_cndmask_b32_e64 v8, v181, 30, s[6:7]
	v_cmp_gt_f32_e64 s[6:7], v9, v10
	s_nop 1
	v_cndmask_b32_e64 v8, v8, 31, s[6:7]
	v_cmp_ne_u32_e64 s[8:9], 0, v8
	s_nop 1
	v_cndmask_b32_e64 v178, v168, v178, s[8:9]
	v_cmp_ne_u32_e64 s[8:9], 1, v8
	v_max_f32_e32 v178, 0xff800000, v178
	s_nop 0
	v_cndmask_b32_e64 v179, v168, v179, s[8:9]
	v_cmp_ne_u32_e64 s[8:9], 2, v8
	s_nop 1
	v_cndmask_b32_e64 v17, v168, v17, s[8:9]
	v_cmp_ne_u32_e64 s[8:9], 3, v8
	s_nop 1
	v_cndmask_b32_e64 v19, v168, v19, s[8:9]
	v_cmp_ne_u32_e64 s[8:9], 4, v8
	s_nop 1
	v_cndmask_b32_e64 v16, v168, v16, s[8:9]
	v_cmp_ne_u32_e64 s[8:9], 5, v8
	s_nop 1
	v_cndmask_b32_e64 v13, v168, v13, s[8:9]
	v_cmp_ne_u32_e64 s[8:9], 6, v8
	s_nop 1
	v_cndmask_b32_e64 v12, v168, v12, s[8:9]
	v_cmp_ne_u32_e64 s[8:9], 7, v8
	s_nop 1
	v_cndmask_b32_e64 v15, v168, v15, s[8:9]
	v_cmp_ne_u32_e64 s[8:9], 8, v8
	s_nop 1
	v_cndmask_b32_e64 v181, v168, v14, s[8:9]
	v_cmp_ne_u32_e64 s[8:9], 9, v8
	s_nop 1
	v_cndmask_b32_e64 v18, v168, v18, s[8:9]
	v_cmp_ne_u32_e64 s[8:9], 10, v8
	s_nop 1
	v_cndmask_b32_e64 v180, v168, v180, s[8:9]
	v_cmp_ne_u32_e64 s[8:9], 11, v8
	s_nop 1
	v_cndmask_b32_e64 v11, v168, v11, s[8:9]
	v_cmp_ne_u32_e64 s[8:9], 12, v8
	s_nop 1
	v_cndmask_b32_e64 v24, v168, v24, s[8:9]
	v_cmp_ne_u32_e64 s[8:9], 13, v8
	s_nop 1
	v_cndmask_b32_e64 v25, v168, v25, s[8:9]
	v_cmp_ne_u32_e64 s[8:9], 14, v8
	s_nop 1
	v_cndmask_b32_e64 v28, v168, v28, s[8:9]
	v_cmp_ne_u32_e64 s[8:9], 15, v8
	s_nop 1
	v_cndmask_b32_e64 v29, v168, v29, s[8:9]
	v_cmp_ne_u32_e64 s[8:9], 16, v8
	s_nop 1
	v_cndmask_b32_e64 v171, v168, v171, s[8:9]
	v_cmp_ne_u32_e64 s[8:9], 17, v8
	s_nop 1
	v_cndmask_b32_e64 v172, v168, v172, s[8:9]
	v_cmp_ne_u32_e64 s[8:9], 18, v8
	s_nop 1
	v_cndmask_b32_e64 v26, v168, v26, s[8:9]
	v_cmp_ne_u32_e64 s[8:9], 19, v8
	s_nop 1
	v_cndmask_b32_e64 v27, v168, v27, s[8:9]
	v_cmp_ne_u32_e64 s[8:9], 20, v8
	s_nop 1
	v_cndmask_b32_e64 v173, v168, v173, s[8:9]
	v_cmp_ne_u32_e64 s[8:9], 21, v8
	s_nop 1
	v_cndmask_b32_e64 v174, v168, v174, s[8:9]
	v_cmp_ne_u32_e64 s[8:9], 22, v8
	s_nop 1
	v_cndmask_b32_e64 v22, v168, v22, s[8:9]
	v_cmp_ne_u32_e64 s[8:9], 23, v8
	s_nop 1
	v_cndmask_b32_e64 v23, v168, v23, s[8:9]
	v_cmp_ne_u32_e64 s[8:9], 24, v8
	s_nop 1
	v_cndmask_b32_e64 v175, v168, v175, s[8:9]
	v_cmp_ne_u32_e64 s[8:9], 25, v8
	s_nop 1
	v_cndmask_b32_e64 v176, v168, v176, s[8:9]
	v_cmp_ne_u32_e64 s[8:9], 26, v8
	s_nop 1
	v_cndmask_b32_e64 v30, v168, v30, s[8:9]
	v_cmp_ne_u32_e64 s[8:9], 27, v8
	s_nop 1
	v_cndmask_b32_e64 v31, v168, v31, s[8:9]
	v_cmp_ne_u32_e64 s[8:9], 28, v8
	s_nop 1
	v_cndmask_b32_e64 v20, v168, v20, s[8:9]
	v_cmp_ne_u32_e64 s[8:9], 29, v8
	s_nop 1
	v_cndmask_b32_e64 v21, v168, v21, s[8:9]
	v_cmp_ne_u32_e64 s[8:9], 30, v8
	s_nop 1
	v_cndmask_b32_e64 v177, v168, v177, s[8:9]
	v_cmp_ne_u32_e64 s[8:9], 31, v8
	s_nop 1
	v_cndmask_b32_e64 v14, v168, v9, s[8:9]
	v_cmp_gt_f32_e64 s[8:9], v179, v178
	s_nop 1
	v_cndmask_b32_e64 v178, v178, v179, s[8:9]
	v_cndmask_b32_e64 v179, 0, 1, s[8:9]
	v_cmp_gt_f32_e64 s[8:9], v17, v178
	s_nop 1
	v_cndmask_b32_e64 v17, v178, v17, s[8:9]
	v_cndmask_b32_e64 v178, v179, 2, s[8:9]
	v_cmp_gt_f32_e64 s[8:9], v19, v17
	s_nop 1
	v_cndmask_b32_e64 v17, v17, v19, s[8:9]
	v_cndmask_b32_e64 v19, v178, 3, s[8:9]
	v_cmp_gt_f32_e64 s[8:9], v16, v17
	s_nop 1
	v_cndmask_b32_e64 v16, v17, v16, s[8:9]
	v_cndmask_b32_e64 v17, v19, 4, s[8:9]
; #define LDS_WAIT() asm volatile("s_waitcnt lgkmcnt(0)" ::: "memory")
; __global__ void __launch_bounds__(NTHREADS, 2) mk_fwd(Args args) {
;     ...
;                     for (int j = 0; j < 32; ++j) if (lg[j] > best) { best = lg[j]; bi = j; }
; #pragma unroll
;                     for (int j = 0; j < 32; ++j) if (j == bi) lg[j] = -INFINITY;
;                     tv[k] = best; ti[k] = bi; }
;                 float ge[4], gs = 0.f;
; #pragma unroll
;                 for (int k = 0; k < 4; ++k) { ge[k] = __expf(tv[k] - tv[0]); gs += ge[k]; }
;                 const float gi = 1.0f / gs;
;                 int rk[4];
; #pragma unroll
;                 for (int k = 0; k < 4; ++k) rk[k] = __hip_atomic_fetch_add(&hist[ti[k]], 1, __ATOMIC_RELAXED, __HIP_MEMORY_SCOPE_WORKGROUP);
;                 LDS_WAIT();
;                 if (F.lane < 32) { const int hc = hist[F.lane]; int bs = 0; if (hc > 0) bs = (int)__hip_atomic_fetch_add(F.ctl + CW_CNT + F.lane, (unsigned)hc, RLX_AGENT); basel[F.lane] = bs; }
	v_cmp_gt_f32_e64 s[8:9], v13, v16
	v_lshl_add_u32 v19, v4, 2, 0
	s_nop 0
	v_cndmask_b32_e64 v13, v16, v13, s[8:9]
	v_cndmask_b32_e64 v16, v17, 5, s[8:9]
	v_cmp_gt_f32_e64 s[8:9], v12, v13
	s_nop 1
	v_cndmask_b32_e64 v12, v13, v12, s[8:9]
	v_cndmask_b32_e64 v13, v16, 6, s[8:9]
	v_cmp_gt_f32_e64 s[8:9], v15, v12
	s_nop 1
	v_cndmask_b32_e64 v12, v12, v15, s[8:9]
	v_cndmask_b32_e64 v13, v13, 7, s[8:9]
	v_cmp_gt_f32_e64 s[8:9], v181, v12
	s_nop 1
	v_cndmask_b32_e64 v12, v12, v181, s[8:9]
	v_cndmask_b32_e64 v13, v13, 8, s[8:9]
	v_cmp_gt_f32_e64 s[8:9], v18, v12
	s_nop 1
	v_cndmask_b32_e64 v12, v12, v18, s[8:9]
	v_cndmask_b32_e64 v13, v13, 9, s[8:9]
	v_cmp_gt_f32_e64 s[8:9], v180, v12
	v_lshl_add_u32 v18, v8, 2, 0
	s_nop 0
	v_cndmask_b32_e64 v12, v12, v180, s[8:9]
	v_cndmask_b32_e64 v13, v13, 10, s[8:9]
	v_cmp_gt_f32_e64 s[8:9], v11, v12
	s_nop 1
	v_cndmask_b32_e64 v11, v12, v11, s[8:9]
	v_cndmask_b32_e64 v12, v13, 11, s[8:9]
	v_cmp_gt_f32_e64 s[8:9], v24, v11
	s_nop 1
	v_cndmask_b32_e64 v11, v11, v24, s[8:9]
	v_cndmask_b32_e64 v12, v12, 12, s[8:9]
	v_cmp_gt_f32_e64 s[8:9], v25, v11
	s_nop 1
	v_cndmask_b32_e64 v11, v11, v25, s[8:9]
	v_cndmask_b32_e64 v12, v12, 13, s[8:9]
	v_cmp_gt_f32_e64 s[8:9], v28, v11
	s_nop 1
	v_cndmask_b32_e64 v11, v11, v28, s[8:9]
	v_cndmask_b32_e64 v12, v12, 14, s[8:9]
	v_cmp_gt_f32_e64 s[8:9], v29, v11
	s_nop 1
	v_cndmask_b32_e64 v11, v11, v29, s[8:9]
	v_cndmask_b32_e64 v12, v12, 15, s[8:9]
	v_cmp_gt_f32_e64 s[8:9], v171, v11
	s_nop 1
	v_cndmask_b32_e64 v11, v11, v171, s[8:9]
	v_cndmask_b32_e64 v12, v12, 16, s[8:9]
	v_cmp_gt_f32_e64 s[8:9], v172, v11
	s_nop 1
	v_cndmask_b32_e64 v11, v11, v172, s[8:9]
	v_cndmask_b32_e64 v12, v12, 17, s[8:9]
	v_cmp_gt_f32_e64 s[8:9], v26, v11
	s_nop 1
	v_cndmask_b32_e64 v11, v11, v26, s[8:9]
	v_cndmask_b32_e64 v12, v12, 18, s[8:9]
	v_cmp_gt_f32_e64 s[8:9], v27, v11
	s_nop 1
	v_cndmask_b32_e64 v11, v11, v27, s[8:9]
	v_cndmask_b32_e64 v12, v12, 19, s[8:9]
	v_cmp_gt_f32_e64 s[8:9], v173, v11
	s_nop 1
	v_cndmask_b32_e64 v11, v11, v173, s[8:9]
	v_cndmask_b32_e64 v12, v12, 20, s[8:9]
	v_cmp_gt_f32_e64 s[8:9], v174, v11
	s_nop 1
	v_cndmask_b32_e64 v11, v11, v174, s[8:9]
	v_cndmask_b32_e64 v12, v12, 21, s[8:9]
	v_cmp_gt_f32_e64 s[8:9], v22, v11
	s_nop 1
	v_cndmask_b32_e64 v11, v11, v22, s[8:9]
	v_cndmask_b32_e64 v12, v12, 22, s[8:9]
	v_cmp_gt_f32_e64 s[8:9], v23, v11
	s_nop 1
	v_cndmask_b32_e64 v11, v11, v23, s[8:9]
	v_cndmask_b32_e64 v12, v12, 23, s[8:9]
	v_cmp_gt_f32_e64 s[8:9], v175, v11
	s_nop 1
	v_cndmask_b32_e64 v11, v11, v175, s[8:9]
	v_cndmask_b32_e64 v12, v12, 24, s[8:9]
	v_cmp_gt_f32_e64 s[8:9], v176, v11
	s_nop 1
	v_cndmask_b32_e64 v11, v11, v176, s[8:9]
	v_cndmask_b32_e64 v12, v12, 25, s[8:9]
	v_cmp_gt_f32_e64 s[8:9], v30, v11
	s_nop 1
	v_cndmask_b32_e64 v11, v11, v30, s[8:9]
	v_cndmask_b32_e64 v12, v12, 26, s[8:9]
	v_cmp_gt_f32_e64 s[8:9], v31, v11
	s_nop 1
	v_cndmask_b32_e64 v11, v11, v31, s[8:9]
	v_cndmask_b32_e64 v12, v12, 27, s[8:9]
	v_cmp_gt_f32_e64 s[8:9], v20, v11
	s_nop 1
	v_cndmask_b32_e64 v11, v11, v20, s[8:9]
	v_cndmask_b32_e64 v12, v12, 28, s[8:9]
	v_cmp_gt_f32_e64 s[8:9], v21, v11
	v_lshl_add_u32 v20, v2, 2, 0
	ds_add_rtn_u32 v16, v20, v166 offset:34816
	v_cndmask_b32_e64 v11, v11, v21, s[8:9]
	v_cndmask_b32_e64 v12, v12, 29, s[8:9]
	v_cmp_gt_f32_e64 s[8:9], v177, v11
	ds_add_rtn_u32 v15, v19, v166 offset:34816
	ds_add_rtn_u32 v13, v18, v166 offset:34816
	v_cndmask_b32_e64 v21, v11, v177, s[8:9]
	v_cndmask_b32_e64 v11, v12, 30, s[8:9]
	v_cmp_gt_f32_e64 s[8:9], v14, v21
	s_nop 1
	v_cndmask_b32_e64 v11, v11, 31, s[8:9]
	v_lshl_add_u32 v17, v11, 2, 0
	ds_add_rtn_u32 v12, v17, v166 offset:34816
	s_waitcnt lgkmcnt(0)
	s_and_saveexec_b64 s[44:45], s[2:3]
	s_cbranch_execz .LBB0_1101
	ds_read_b32 v23, v169 offset:34816
	v_mov_b32_e32 v22, 0
	s_waitcnt lgkmcnt(0)
	v_cmp_lt_i32_e64 s[10:11], 0, v23
	s_and_saveexec_b64 s[46:47], s[10:11]
	s_cbranch_execz .LBB0_1100
	global_atomic_add v22, v[38:39], v23, off sc0
	s_branch .LBB0_1100
